# static s_setprio 1 for waves 4-7 across the attention/conversion ticket loop (reset after the loop)
# speedup vs baseline: 1.0103x; 1.0103x over previous
; __device__ __forceinline__ Ptrs make_ptrs(const Args& args, unsigned char* ws0) {
;     int z = 0; asm volatile("" : "+s"(z));
;     const float* const* in = args.in + z;
;     unsigned char* ws = ws0 + z;
;     Ptrs P;
;     P.x = in[0]; P.attn_norm = in[1]; P.w_in = in[2]; P.q_gain = in[3]; P.k_gain = in[4]; P.out_gain = in[5]; P.w_out = in[6]; P.ffn_norm = in[7];
;     P.dwg = in[8]; P.dwu = in[9]; P.dwd = in[10]; P.router = in[11]; P.mwg = in[12]; P.mwu = in[13]; P.mwd = in[14];
;     P.out = args.out; P.ctl = (gu32*)(ws + WS_CTL);
;     P.Wqkv_t = (bf16*)(ws + WS_WQKV); P.Wo_t = (bf16*)(ws + WS_WO); P.Wgu_d = ws + WS_WGU_D; P.Wd_d = ws + WS_WD_D; P.Wgu_m = ws + WS_WGU_M; P.Wd_m = ws + WS_WD_M;
;     P.QKV = (bf16*)(ws + WS_QKV); P.OB = (bf16*)(ws + WS_O); P.AB = (bf16*)(ws + WS_A); P.AB8 = ws + WS_A; P.ACT = ws + WS_ACT; P.XS = ws + WS_XS;
;     P.H = (bf16*)(ws + WS_H); P.YS = (bf16*)(ws + WS_YS); P.kmean = (float*)(ws + WS_MISC + MISC_KMEAN); P.DPO = (bf16*)(ws + WS_DPO); P.DPL = (float*)(ws + WS_DPL);
;     P.rsq = (float*)(ws + WS_MISC + MISC_RSQ); P.Wv8 = ws + WS_WV8;
;     P.sel_e = (unsigned*)(ws + WS_MISC + MISC_SELE); P.sel_rel = (int*)(ws + WS_MISC + MISC_SELREL); P.sel_g = (float*)(ws + WS_MISC + MISC_SELG); P.sel_pos = (int*)(ws + WS_MISC + MISC_SELPOS);
;     return P;
; __global__ void __launch_bounds__(NWAVES * 64, 2) hybrid_fwd(Args args) {
;     ...
;             const Ptrs P = make_ptrs(args, ws0);
;             const att::AttnArgs AA{P.QKV, P.OB, P.kmean, P.out_gain + layer * D, P.DPO, P.DPL, (unsigned*)((unsigned char*)P.DPL + (WS_MLIST - WS_DPL)) + (size_t)layer * att::N_SEL * att::MLCAP, (unsigned*)(P.ctl + CW_MCNT + 256 * (layer + args.qoff)), (unsigned*)(P.ctl + CW_MDONE + 64 * (layer + args.qoff)), (layer == WO8_LAYER) ? 1 : 0};
;     ...
;             attn_conv_phase(P, AA, layer, (unsigned*)(P.ctl + CW_ATTQ + 64 * (layer + args.qoff)), lds, wave);
.LBB0_434:
	s_or_b64 exec, exec, s[14:15]
	s_add_u32 s3, s20, 0x8300000
	s_addc_u32 s81, s21, 0
	v_writelane_b32 v254, s3, 57
	s_add_u32 s3, s20, 0x1e300000
	v_writelane_b32 v254, s3, 58
	s_addc_u32 s3, s21, 0
	s_add_u32 s38, s20, 0x2d300000
	s_addc_u32 s39, s21, 0
	v_writelane_b32 v254, s3, 59
	s_add_u32 s3, s20, 0x33300000
	v_writelane_b32 v254, s3, 60
	s_addc_u32 s3, s21, 0
	v_writelane_b32 v254, s3, 61
	s_add_u32 s3, s20, 0x48100000
	v_writelane_b32 v254, s3, 62
	s_addc_u32 s3, s21, 0
	s_add_u32 s92, s20, 0x48200000
	s_addc_u32 s93, s21, 0
	s_add_u32 s14, s20, 0x4da00000
	s_addc_u32 s15, s21, 0
	v_writelane_b32 v255, s14, 0
	v_writelane_b32 v254, s3, 63
	s_nop 0
	v_writelane_b32 v255, s15, 1
	s_add_u32 s14, s20, 0x4e100000
	s_addc_u32 s15, s21, 0
	v_writelane_b32 v255, s14, 2
	s_nop 1
	v_writelane_b32 v255, s15, 3
	s_lshl_b32 s14, s80, 11
	s_mov_b32 s15, s90
	s_lshl_b64 s[14:15], s[14:15], 2
	s_add_u32 s14, s44, s14
	s_addc_u32 s15, s45, s15
	v_writelane_b32 v255, s14, 6
	s_nop 1
	v_writelane_b32 v255, s15, 7
	s_mul_i32 s14, s80, 0x8ca00
	s_mov_b32 s15, s90
	s_lshl_b64 s[14:15], s[14:15], 2
	s_add_u32 s14, s20, s14
	s_addc_u32 s15, s21, s15
	s_add_u32 s14, s14, 0x4dc00000
	s_addc_u32 s15, s15, 0
	v_writelane_b32 v255, s14, 8
	s_nop 1
	v_writelane_b32 v255, s15, 9
	s_lshl_b32 s14, s22, 8
	s_ashr_i32 s15, s14, 31
	s_lshl_b64 s[14:15], s[14:15], 2
	s_add_u32 s14, s20, s14
	s_addc_u32 s15, s21, s15
	s_add_u32 s14, s14, 0x9000
	s_addc_u32 s15, s15, 0
	s_add_u32 s0, s20, s0
	s_addc_u32 s1, s21, s1
	s_add_u32 s78, s0, 0xa000
	s_addc_u32 s79, s1, 0
	v_writelane_b32 v255, s14, 10
	s_add_u32 s0, s46, 0x1000000
	s_addc_u32 s1, s47, 0
	v_writelane_b32 v255, s15, 11
	v_writelane_b32 v255, s0, 12
	s_nop 1
	v_writelane_b32 v255, s1, 13
	s_add_u32 s0, s20, 0x3900000
	s_addc_u32 s1, s21, 0
	v_writelane_b32 v255, s0, 14
	s_mov_b64 s[20:21], 0
	s_nop 0
	v_writelane_b32 v255, s1, 15
	s_add_u32 s0, s40, 0x2000
	s_addc_u32 s1, s41, 0
	v_writelane_b32 v255, s0, 16
	s_nop 1
	v_writelane_b32 v255, s1, 17
	s_add_u32 s0, s42, 0x3000000
	s_addc_u32 s1, s43, 0
	v_writelane_b32 v255, s0, 18
	s_nop 1
	v_writelane_b32 v255, s1, 19
	v_writelane_b32 v255, s38, 20
	s_nop 1
	v_writelane_b32 v255, s39, 21
	v_writelane_b32 v255, s78, 22
	s_nop 1
	v_writelane_b32 v255, s79, 23
	s_cmpk_ge_u32 s94, 0x100
	s_cbranch_scc0 .Lprio_att_done
	s_setprio 1
.Lprio_att_done:
	s_branch .LBB0_440
.LBB0_435:
	s_or_b64 exec, exec, s[0:1]

; #define XB_IS_T0 (b.wv == 0 && lane_id() == 0)
; #define SEAM(a, b) do { if (PH(a) && PH(b)) { int zb_ = 0; asm volatile("" : "+s"(zb_)); XcdBarrier b2_ = bar; b2_.bar = bar.bar + zb_; xcd_barrier(b2_); } } while (0)
; __device__ __forceinline__ void xcd_barrier(const XcdBarrier& b) {
;     asm volatile("s_waitcnt vmcnt(0)" ::: "memory");
;     __syncthreads();
;     if (XB_IS_T0) {
;         unsigned* bar = b.bar;
;         __builtin_amdgcn_s_waitcnt(0);
;         unsigned nloc = b.st[0], nx = b.st[1];
;         if (nloc == 0u) { xcd_barrier_complete(bar, b.x, nloc, nx); b.st[0] = nloc; b.st[1] = nx; }
; __global__ void __launch_bounds__(NWAVES * 64, 2) hybrid_fwd(Args args) {
;     ...
;         SEAM(PB + 3, PB + 4);
.LBB0_1159:
	s_setprio 0
	s_mul_i32 s0, s80, 11
	s_add_i32 s38, s0, 4
	s_cmp_ge_i32 s38, s77
	s_cbranch_scc1 .LBB0_1172
	s_mov_b32 s14, s90
	s_waitcnt vmcnt(0)
	v_readlane_b32 s0, v254, 55
	v_readlane_b32 s1, v254, 56
	v_readlane_b32 s88, v254, 25
	s_and_b64 vcc, exec, s[0:1]
	v_readlane_b32 s86, v254, 24
	v_readlane_b32 s89, v254, 26
	v_readlane_b32 s87, v254, 27
	s_waitcnt vmcnt(63) expcnt(7) lgkmcnt(15)
	s_barrier
	s_cbranch_vccnz .LBB0_1215
	v_mbcnt_lo_u32_b32 v0, -1, 0
	v_mbcnt_hi_u32_b32 v0, -1, v0
	s_nop 0
	v_cmp_eq_u32_e32 vcc, 0, v0
	s_and_saveexec_b64 s[0:1], vcc
	s_cbranch_execz .LBB0_1214
	s_ashr_i32 s15, s14, 31
	v_readlane_b32 s16, v254, 5
	s_lshl_b64 s[14:15], s[14:15], 2
	s_waitcnt vmcnt(0) expcnt(0) lgkmcnt(0)
	v_mov_b32_e32 v0, s16
	v_readlane_b32 s16, v251, 5
	ds_read_b32 v3, v0
	s_add_u32 s14, s16, s14
	v_readlane_b32 s16, v254, 6
	v_readlane_b32 s17, v251, 6
	s_addc_u32 s15, s17, s15
	v_mov_b32_e32 v0, s16
	ds_read_b32 v2, v0
	s_waitcnt lgkmcnt(1)
	v_cmp_ne_u32_e32 vcc, 0, v3
	s_cbranch_vccnz .LBB0_1178
	v_readlane_b32 s16, v251, 0
	v_readlane_b32 s17, v251, 1
	s_load_dwordx2 s[18:19], s[16:17], 0x4
	s_add_u32 s16, s14, 0x1000
	s_addc_u32 s17, s15, 0
	s_add_u32 s20, s14, 0x1100
	s_addc_u32 s21, s15, 0
	s_add_u32 s22, s14, 0x1200
	s_addc_u32 s23, s15, 0
	s_waitcnt lgkmcnt(0)
	s_mul_i32 s30, s18, s87
	s_add_u32 s24, s14, 0x1300
	s_mul_i32 s30, s30, s19
	s_addc_u32 s25, s15, 0
	s_mov_b32 s31, 1
	s_branch .LBB0_1165
